# gathered MoE GEMM: next-tile row-index loads issued without per-load vmcnt(0) drains, offsets formed in the K loop; plus residual-epilogue de-serialisation and MLA loop reorder
# speedup vs baseline: 1.0056x; 1.0033x over previous
; #define PG8_VOFFS(vo, unit) do { if constexpr (GATHER) { _Pragma("unroll") for (int _h = 0; _h < 2; ++_h) _Pragma("unroll") for (int _i = 0; _i < 2; ++_i) \
;         (vo)[_h][_i] = (unsigned)(g.gidx[(unit).pm * BM + _h * HALF + RA[_i]] * g.lda + CA[_i]) * 2u; } } while (0)
; #define a launder(kargs)
;     __device__ bool next(int i, Unit& u) const {
;         const int L = i * G + c; if (L >= 16 * nrt * NJ) return false;
;         const int e = L / (nrt * NJ), rem = L - e * (nrt * NJ), rt = rem / NJ, j = rem - rt * NJ;
;         u.pm = (rt < 32) ? (((rt >> 2) * 16 + e) * 4 + (rt & 3)) : (512 + e);
;         u.pn = e * NJ + j; return true;
;     }
; template <class Epi, class Sched, bool GATHER = false>
; __device__ __forceinline__ void gemm_phase(LAS unsigned char* lds, const Gemm g, const Sched& S, const Epi& E) {
;     ...
;     Unit cur, nxt; int ui = 0;
;     if (!S.next(0, cur)) return;
;     f32x4 acc[2][2][4][2];
; #pragma unroll
;     for (int a = 0; a < 2; ++a)
; #pragma unroll
;         for (int b = 0; b < 2; ++b)
; #pragma unroll
;             for (int m = 0; m < 4; ++m)
; #pragma unroll
;                 for (int n = 0; n < 2; ++n) acc[a][b][m][n] = (f32x4){0.f, 0.f, 0.f, 0.f};
;     bf16x8 At[4][2], B0[2][2], B1[2][2];
;     PG8_VOFFS(voC, cur);
;     const char* cA = GATHER ? (const char*)g.A : (const char*)g.A + (size_t)cur.pm * tstepA; const char* cB = (const char*)g.Bt + (size_t)cur.pn * tstepB;
.LBB0_1383:
	s_or_b64 exec, exec, s[4:5]
	v_mov_b32_e32 v244, 0
	v_mov_b32_e32 v245, 0
	v_mov_b32_e32 v246, 0
	v_mov_b32_e32 v247, 0
	s_and_b64 s[4:5], s[36:37], exec
	s_cselect_b32 s3, 32, 33
	v_mov_b32_e32 v6, v0
	s_lshl_b32 s24, s3, 7
	s_waitcnt lgkmcnt(0)
	s_barrier
	s_cmp_ge_i32 s2, s24
	v_readfirstlane_b32 s16, v6
	s_cbranch_scc1 .LBB0_1409
	s_lshl_b32 s25, s3, 3
	v_cvt_f32_u32_e32 v1, s25
	s_sub_i32 s6, 0, s25
	s_abs_i32 s5, s2
	s_ashr_i32 s4, s2, 31
	v_rcp_iflag_f32_e32 v1, v1
	s_nop 0
	v_mul_f32_e32 v1, 0x4f7ffffe, v1
	v_cvt_u32_f32_e32 v1, v1
	s_nop 0
	v_readfirstlane_b32 s36, v1
	s_mul_i32 s6, s6, s36
	s_mul_hi_u32 s6, s36, s6
	s_add_i32 s36, s36, s6
	s_mul_hi_u32 s6, s5, s36
	s_mul_i32 s7, s6, s25
	s_sub_i32 s5, s5, s7
	s_add_i32 s8, s6, 1
	s_sub_i32 s7, s5, s25
	s_cmp_ge_u32 s5, s25
	s_cselect_b32 s6, s8, s6
	s_cselect_b32 s5, s7, s5
	s_add_i32 s7, s6, 1
	s_cmp_ge_u32 s5, s25
	s_cselect_b32 s5, s7, s6
	s_xor_b32 s5, s5, s4
	s_sub_i32 s10, s5, s4
	s_mul_i32 s4, s10, s25
	s_sub_i32 s11, s2, s4
	s_cmpk_gt_i32 s11, 0xff
	s_mov_b64 s[4:5], -1
	s_cbranch_scc0 .LBB0_1386
	s_add_i32 s48, s10, 0x200
	s_mov_b64 s[4:5], 0

; #define PG8_VOFFS(vo, unit) do { if constexpr (GATHER) { _Pragma("unroll") for (int _h = 0; _h < 2; ++_h) _Pragma("unroll") for (int _i = 0; _i < 2; ++_i) \
;         (vo)[_h][_i] = (unsigned)(g.gidx[(unit).pm * BM + _h * HALF + RA[_i]] * g.lda + CA[_i]) * 2u; } } while (0)
; template <class Epi, class Sched, bool GATHER = false>
; __device__ __forceinline__ void gemm_phase(LAS unsigned char* lds, const Gemm g, const Sched& S, const Epi& E) {
;     ...
;         if constexpr (GATHER) { if (has_next) { PG8_VOFFS(voN, nxt); } else {
; #pragma unroll
;             for (int _h = 0; _h < 2; ++_h)
; #pragma unroll
;                 for (int _i = 0; _i < 2; ++_i) voN[_h][_i] = voC[_h][_i]; } }
.LBB0_1399:
	v_cndmask_b32_e64 v2, 0, 1, s[28:29]
	v_cmp_ne_u32_e64 s[4:5], 1, v2
	s_andn2_b64 vcc, exec, s[28:29]
	v_mov_b32_e32 v152, v134
	v_mov_b32_e32 v153, v136
	v_mov_b32_e32 v154, v138
	v_mov_b32_e32 v155, v140
	s_cbranch_vccnz .LBB0_1401
	s_lshl_b32 s19, s47, 8
	v_add_u32_e32 v2, s19, v1
	v_ashrrev_i32_e32 v3, 31, v2
	v_lshl_add_u64 v[2:3], v[2:3], 2, s[8:9]
	global_load_dword v244, v[2:3], off
	v_add_u32_e32 v2, s19, v147
	v_ashrrev_i32_e32 v3, 31, v2
	v_lshl_add_u64 v[2:3], v[2:3], 2, s[8:9]
	global_load_dword v245, v[2:3], off
	s_bitset1_b32 s19, 7
	v_add_u32_e32 v2, s19, v1
	v_ashrrev_i32_e32 v3, 31, v2
	v_lshl_add_u64 v[2:3], v[2:3], 2, s[8:9]
	global_load_dword v246, v[2:3], off
	v_add_u32_e32 v2, s19, v147
	v_ashrrev_i32_e32 v3, 31, v2
	v_lshl_add_u64 v[2:3], v[2:3], 2, s[8:9]
	global_load_dword v247, v[2:3], off

; #define PG8_STAGE_B(bufoff, gbase) do { _Pragma("unroll") for (int _i = 0; _i < 2; ++_i) \
;         __builtin_amdgcn_global_load_lds((const unsigned*)((const char*)(gbase) + voffB[_i]), (LAS unsigned*)(lds + (bufoff) + ldsw + _i * 8192), 16, 0, 0); } while (0)
; #define PG8_LDA(dst, b, h) do { _Pragma("unroll") for (int m = 0; m < 4; ++m) _Pragma("unroll") for (int k = 0; k < 2; ++k) dst[m][k] = *(const LAS bf16x8*)(lds + PG8_SA(b, h) + aoff + m * 2048 + k * 1024); } while (0)
; #define PG8_LDB(dst, b, h) do { _Pragma("unroll") for (int n = 0; n < 2; ++n) _Pragma("unroll") for (int k = 0; k < 2; ++k) dst[n][k] = *(const LAS bf16x8*)(lds + PG8_SB(b, h) + boff + n * 2048 + k * 1024); } while (0)
; #define PG8_MMA(ai, bj, At, Bt) do { __builtin_amdgcn_s_setprio(1); _Pragma("unroll") for (int m = 0; m < 4; ++m) _Pragma("unroll") for (int n = 0; n < 2; ++n) _Pragma("unroll") for (int k = 0; k < 2; ++k) \
;         acc[ai][bj][m][n] = __builtin_amdgcn_mfma_f32_16x16x32_bf16(Bt[n][k], At[m][k], acc[ai][bj][m][n], 0, 0, 0); __builtin_amdgcn_s_setprio(0); } while (0)
; template <class Epi, class Sched, bool GATHER = false>
; __device__ __forceinline__ void gemm_phase(LAS unsigned char* lds, const Gemm g, const Sched& S, const Epi& E) {
;     ...
;         for (int t = 0; t < nt; t += 2) {
;             const bool last = (t == nt - 2);
;             const char* a1 = cA + (size_t)(t + 1) * kstep;
;             const char* a2 = last ? nA : cA + (size_t)(t + 2) * kstep; const char* b2 = last ? nB : cB + (size_t)(t + 2) * kstep;
;             const char* a3 = a2 + kstep; const char* b3 = b2 + kstep;
;             unsigned vo2[2][2];
;             if constexpr (GATHER) {
; #pragma unroll
;             for (int _h = 0; _h < 2; ++_h)
; #pragma unroll
;                 for (int _i = 0; _i < 2; ++_i) vo2[_h][_i] = last ? voN[_h][_i] : voC[_h][_i]; }
;             PG8_LDB(B0, 0, 0); PG8_LDB(B1, 0, 1); PG8_SCHED; PG8_LDA(At, 0, 0); PG8_STAGE_A(PG8_SA(1, 1), a1, voC, 1);
;             PG8_WAIT_V(8); PG8_WAIT_L(0); PG8_BAR; PG8_MMA(0, 0, At, B0); PG8_MMA(0, 1, At, B1); PG8_BAR; PG8_SCHED;
;             PG8_LDA(At, 0, 1); PG8_STAGE_B(PG8_SB(0, 0), b2); PG8_STAGE_B(PG8_SB(0, 1), b2 + hstepB); PG8_STAGE_A(PG8_SA(0, 0), a2, vo2, 0);
;             PG8_WAIT_V(8); PG8_WAIT_L(0); PG8_BAR; PG8_MMA(1, 0, At, B0); PG8_MMA(1, 1, At, B1); PG8_BAR; PG8_SCHED;
.LBB0_1402:
	s_add_u32 s28, s34, s26
	s_addc_u32 s29, s35, s27
	s_add_u32 s30, s28, 0x81ee400
	s_addc_u32 s31, s29, 0
	s_add_u32 s53, s50, s26
	s_addc_u32 s54, s51, s27
	s_cmpk_eq_i32 s26, 0x700
	s_cselect_b64 vcc, -1, 0
	s_and_b64 s[28:29], vcc, exec
	s_cselect_b32 s31, s7, s31
	s_cselect_b32 s30, s6, s30
	s_cselect_b32 s29, s19, s54
	s_cselect_b32 s28, s49, s53
	s_add_i32 s53, 0, 0x10000
	v_add_u32_e32 v141, s53, v150
	s_add_i32 s58, 0, 0x14000
	ds_read_b128 v[156:159], v141
	ds_read_b128 v[160:163], v141 offset:1024
	ds_read_b128 v[164:167], v141 offset:2048
	ds_read_b128 v[168:171], v141 offset:3072
	v_add_u32_e32 v141, s58, v150
	ds_read_b128 v[172:175], v141
	ds_read_b128 v[176:179], v141 offset:1024
	ds_read_b128 v[180:183], v141 offset:2048
	ds_read_b128 v[184:187], v141 offset:3072
	v_lshl_add_u32 v152, v244, 11, v146
	v_lshl_add_u32 v153, v245, 11, v148
	v_lshl_add_u32 v154, v246, 11, v146
	v_lshl_add_u32 v155, v247, 11, v148
	v_cndmask_b32_e32 v194, v134, v152, vcc
	v_cndmask_b32_e32 v192, v136, v153, vcc
	v_cndmask_b32_e32 v135, v138, v154, vcc
	v_cndmask_b32_e32 v139, v140, v155, vcc
	v_lshl_add_u64 v[236:237], v[144:145], 0, s[26:27]
	s_add_i32 m0, s23, 0xc000
	ds_read_b128 v[188:191], v151
	ds_read_b128 v[198:201], v151 offset:1024
	ds_read_b128 v[204:207], v151 offset:2048
	ds_read_b128 v[208:211], v151 offset:3072
	ds_read_b128 v[212:215], v151 offset:4096
	ds_read_b128 v[216:219], v151 offset:5120
	ds_read_b128 v[220:223], v151 offset:6144
	ds_read_b128 v[228:231], v151 offset:7168
	global_load_lds_dwordx4 v[236:237], off
	v_lshl_add_u64 v[236:237], v[142:143], 0, s[26:27]
	s_add_i32 m0, s23, 0xe000
	s_nop 0
	global_load_lds_dwordx4 v[236:237], off
	s_waitcnt vmcnt(8)
	s_waitcnt lgkmcnt(0)
	s_barrier
	s_setprio 1
	s_waitcnt lgkmcnt(0)
	v_mfma_f32_16x16x32_bf16 v[126:129], v[156:159], v[188:191], v[126:129]
	v_mfma_f32_16x16x32_bf16 v[122:125], v[164:167], v[188:191], v[122:125]
	v_mfma_f32_16x16x32_bf16 v[110:113], v[156:159], v[204:207], v[110:113]
	v_mfma_f32_16x16x32_bf16 v[106:109], v[164:167], v[204:207], v[106:109]
	v_mfma_f32_16x16x32_bf16 v[94:97], v[156:159], v[212:215], v[94:97]
	v_mfma_f32_16x16x32_bf16 v[90:93], v[164:167], v[212:215], v[90:93]
	v_mfma_f32_16x16x32_bf16 v[78:81], v[156:159], v[220:223], v[78:81]
	v_mfma_f32_16x16x32_bf16 v[74:77], v[164:167], v[220:223], v[74:77]
	v_mfma_f32_16x16x32_bf16 v[126:129], v[160:163], v[198:201], v[126:129]
	v_mfma_f32_16x16x32_bf16 v[122:125], v[168:171], v[198:201], v[122:125]
	v_mfma_f32_16x16x32_bf16 v[110:113], v[160:163], v[208:211], v[110:113]
	v_mfma_f32_16x16x32_bf16 v[106:109], v[168:171], v[208:211], v[106:109]
	v_mfma_f32_16x16x32_bf16 v[94:97], v[160:163], v[216:219], v[94:97]
	v_mfma_f32_16x16x32_bf16 v[90:93], v[168:171], v[216:219], v[90:93]
	v_mfma_f32_16x16x32_bf16 v[78:81], v[160:163], v[228:231], v[78:81]
	v_mfma_f32_16x16x32_bf16 v[74:77], v[168:171], v[228:231], v[74:77]
	s_setprio 0
	s_setprio 1
	v_mfma_f32_16x16x32_bf16 v[118:121], v[172:175], v[188:191], v[118:121]
	v_mfma_f32_16x16x32_bf16 v[114:117], v[180:183], v[188:191], v[114:117]
	v_mfma_f32_16x16x32_bf16 v[102:105], v[172:175], v[204:207], v[102:105]
	v_mfma_f32_16x16x32_bf16 v[98:101], v[180:183], v[204:207], v[98:101]
	v_mfma_f32_16x16x32_bf16 v[86:89], v[172:175], v[212:215], v[86:89]
	v_mfma_f32_16x16x32_bf16 v[82:85], v[180:183], v[212:215], v[82:85]
	v_mfma_f32_16x16x32_bf16 v[70:73], v[172:175], v[220:223], v[70:73]
	v_mfma_f32_16x16x32_bf16 v[66:69], v[180:183], v[220:223], v[66:69]
	v_mfma_f32_16x16x32_bf16 v[118:121], v[176:179], v[198:201], v[118:121]
	v_mfma_f32_16x16x32_bf16 v[114:117], v[184:187], v[198:201], v[114:117]
	v_mfma_f32_16x16x32_bf16 v[102:105], v[176:179], v[208:211], v[102:105]
	v_mfma_f32_16x16x32_bf16 v[98:101], v[184:187], v[208:211], v[98:101]
	v_mfma_f32_16x16x32_bf16 v[86:89], v[176:179], v[216:219], v[86:89]
	v_mfma_f32_16x16x32_bf16 v[82:85], v[184:187], v[216:219], v[82:85]
	v_mfma_f32_16x16x32_bf16 v[70:73], v[176:179], v[228:231], v[70:73]
	v_mfma_f32_16x16x32_bf16 v[66:69], v[184:187], v[228:231], v[66:69]
	s_setprio 0
	s_barrier
	s_add_i32 s53, s53, s40
	v_lshl_add_u64 v[236:237], s[28:29], 0, v[130:131]
	s_mov_b32 m0, s53
	ds_read_b128 v[188:191], v151 offset:16384
	ds_read_b128 v[198:201], v151 offset:17408
	ds_read_b128 v[204:207], v151 offset:18432
	ds_read_b128 v[208:211], v151 offset:19456
	ds_read_b128 v[212:215], v151 offset:20480
	ds_read_b128 v[216:219], v151 offset:21504
	ds_read_b128 v[220:223], v151 offset:22528
	ds_read_b128 v[228:231], v151 offset:23552
	global_load_lds_dwordx4 v[236:237], off
	s_add_i32 m0, s53, 0x2000
	s_add_u32 s54, s28, 0x40000
	v_lshl_add_u64 v[238:239], s[28:29], 0, v[132:133]
	s_addc_u32 s55, s29, 0
	s_add_i32 s53, s58, s40
	global_load_lds_dwordx4 v[238:239], off
	v_lshl_add_u64 v[240:241], s[54:55], 0, v[130:131]
	s_mov_b32 m0, s53
	v_mov_b32_e32 v193, v195
	global_load_lds_dwordx4 v[240:241], off
	v_lshl_add_u64 v[240:241], s[54:55], 0, v[132:133]
	s_add_i32 m0, s53, 0x2000
	s_nop 0
	global_load_lds_dwordx4 v[240:241], off
	s_mov_b32 m0, s23
	v_lshl_add_u64 v[240:241], s[30:31], 0, v[194:195]
	global_load_lds_dwordx4 v194, s[30:31]
	s_mov_b32 m0, s41
	s_nop 0
	global_load_lds_dwordx4 v192, s[30:31]
	s_waitcnt vmcnt(8)
	s_waitcnt lgkmcnt(0)
	v_lshl_add_u64 v[192:193], s[30:31], 0, v[192:193]
	s_barrier
; #define PG8_LDA(dst, b, h) do { _Pragma("unroll") for (int m = 0; m < 4; ++m) _Pragma("unroll") for (int k = 0; k < 2; ++k) dst[m][k] = *(const LAS bf16x8*)(lds + PG8_SA(b, h) + aoff + m * 2048 + k * 1024); } while (0)
; #define PG8_LDB(dst, b, h) do { _Pragma("unroll") for (int n = 0; n < 2; ++n) _Pragma("unroll") for (int k = 0; k < 2; ++k) dst[n][k] = *(const LAS bf16x8*)(lds + PG8_SB(b, h) + boff + n * 2048 + k * 1024); } while (0)
; #define PG8_MMA(ai, bj, At, Bt) do { __builtin_amdgcn_s_setprio(1); _Pragma("unroll") for (int m = 0; m < 4; ++m) _Pragma("unroll") for (int n = 0; n < 2; ++n) _Pragma("unroll") for (int k = 0; k < 2; ++k) \
;         acc[ai][bj][m][n] = __builtin_amdgcn_mfma_f32_16x16x32_bf16(Bt[n][k], At[m][k], acc[ai][bj][m][n], 0, 0, 0); __builtin_amdgcn_s_setprio(0); } while (0)
; #define PG8_WAIT_V(n) asm volatile("s_waitcnt vmcnt(" #n ")" ::: "memory")
; #define PG8_WAIT_L(n) asm volatile("s_waitcnt lgkmcnt(" #n ")" ::: "memory")
; #define PG8_BAR __builtin_amdgcn_s_barrier()
; #define PG8_SCHED __builtin_amdgcn_sched_barrier(0)
; template <class Epi, class Sched, bool GATHER = false>
; __device__ __forceinline__ void gemm_phase(LAS unsigned char* lds, const Gemm g, const Sched& S, const Epi& E) {
;     ...
;             PG8_WAIT_V(8); PG8_WAIT_L(0); PG8_BAR; PG8_MMA(1, 0, At, B0); PG8_MMA(1, 1, At, B1); PG8_BAR; PG8_SCHED;
;             PG8_LDB(B0, 1, 0); PG8_LDB(B1, 1, 1); PG8_SCHED; PG8_LDA(At, 1, 0); PG8_STAGE_A(PG8_SA(0, 1), a2, vo2, 1);
;             PG8_WAIT_V(8); PG8_WAIT_L(0); PG8_BAR; PG8_MMA(0, 0, At, B0); PG8_MMA(0, 1, At, B1); PG8_BAR; PG8_SCHED;
	s_setprio 1
	s_waitcnt lgkmcnt(0)
	v_mfma_f32_16x16x32_bf16 v[62:65], v[156:159], v[188:191], v[62:65]
	v_mfma_f32_16x16x32_bf16 v[58:61], v[164:167], v[188:191], v[58:61]
	v_mfma_f32_16x16x32_bf16 v[46:49], v[156:159], v[204:207], v[46:49]
	v_mfma_f32_16x16x32_bf16 v[42:45], v[164:167], v[204:207], v[42:45]
	v_mfma_f32_16x16x32_bf16 v[30:33], v[156:159], v[212:215], v[30:33]
	v_mfma_f32_16x16x32_bf16 v[26:29], v[164:167], v[212:215], v[26:29]
	v_mfma_f32_16x16x32_bf16 v[14:17], v[156:159], v[220:223], v[14:17]
	v_mfma_f32_16x16x32_bf16 v[10:13], v[164:167], v[220:223], v[10:13]
	v_mfma_f32_16x16x32_bf16 v[62:65], v[160:163], v[198:201], v[62:65]
	v_mfma_f32_16x16x32_bf16 v[58:61], v[168:171], v[198:201], v[58:61]
	v_mfma_f32_16x16x32_bf16 v[46:49], v[160:163], v[208:211], v[46:49]
	v_mfma_f32_16x16x32_bf16 v[42:45], v[168:171], v[208:211], v[42:45]
	v_mfma_f32_16x16x32_bf16 v[30:33], v[160:163], v[216:219], v[30:33]
	v_mfma_f32_16x16x32_bf16 v[26:29], v[168:171], v[216:219], v[26:29]
	v_mfma_f32_16x16x32_bf16 v[14:17], v[160:163], v[228:231], v[14:17]
	v_mfma_f32_16x16x32_bf16 v[10:13], v[168:171], v[228:231], v[10:13]
	s_setprio 0
	s_setprio 1
	v_mfma_f32_16x16x32_bf16 v[54:57], v[172:175], v[188:191], v[54:57]
	v_mfma_f32_16x16x32_bf16 v[50:53], v[180:183], v[188:191], v[50:53]
	v_mfma_f32_16x16x32_bf16 v[38:41], v[172:175], v[204:207], v[38:41]
	v_mfma_f32_16x16x32_bf16 v[34:37], v[180:183], v[204:207], v[34:37]
	v_mfma_f32_16x16x32_bf16 v[22:25], v[172:175], v[212:215], v[22:25]
	v_mfma_f32_16x16x32_bf16 v[18:21], v[180:183], v[212:215], v[18:21]
	v_mfma_f32_16x16x32_bf16 v[6:9], v[172:175], v[220:223], v[6:9]
	v_mfma_f32_16x16x32_bf16 v[2:5], v[180:183], v[220:223], v[2:5]
	v_mfma_f32_16x16x32_bf16 v[54:57], v[176:179], v[198:201], v[54:57]
	v_mfma_f32_16x16x32_bf16 v[50:53], v[184:187], v[198:201], v[50:53]
	v_mfma_f32_16x16x32_bf16 v[38:41], v[176:179], v[208:211], v[38:41]
	v_mfma_f32_16x16x32_bf16 v[34:37], v[184:187], v[208:211], v[34:37]
	v_mfma_f32_16x16x32_bf16 v[22:25], v[176:179], v[216:219], v[22:25]
	v_mfma_f32_16x16x32_bf16 v[18:21], v[184:187], v[216:219], v[18:21]
	v_mfma_f32_16x16x32_bf16 v[6:9], v[176:179], v[228:231], v[6:9]
	v_mfma_f32_16x16x32_bf16 v[2:5], v[184:187], v[228:231], v[2:5]
	s_setprio 0
	s_barrier
	s_add_i32 s53, 0, 0x18000
	v_add_u32_e32 v141, s53, v150
	s_add_i32 s54, 0, 0x1c000
	ds_read_b128 v[156:159], v141
	ds_read_b128 v[160:163], v141 offset:1024
	ds_read_b128 v[164:167], v141 offset:2048
	ds_read_b128 v[168:171], v141 offset:3072
	v_add_u32_e32 v141, s54, v150
	ds_read_b128 v[172:175], v141
	ds_read_b128 v[176:179], v141 offset:1024
	ds_read_b128 v[180:183], v141 offset:2048
	ds_read_b128 v[184:187], v141 offset:3072
	s_mov_b32 m0, s42
	ds_read_b128 v[188:191], v151 offset:32768
	ds_read_b128 v[198:201], v151 offset:33792
	ds_read_b128 v[204:207], v151 offset:34816
	ds_read_b128 v[208:211], v151 offset:35840
	ds_read_b128 v[212:215], v151 offset:36864
	ds_read_b128 v[216:219], v151 offset:37888
	ds_read_b128 v[220:223], v151 offset:38912
	ds_read_b128 v[228:231], v151 offset:39936
	global_load_lds_dwordx4 v135, s[30:31]
	s_mov_b32 m0, s43
	s_nop 0
	global_load_lds_dwordx4 v139, s[30:31]
	s_waitcnt vmcnt(8)
	s_waitcnt lgkmcnt(0)
	s_barrier
	s_setprio 1
	s_waitcnt lgkmcnt(0)
	v_mfma_f32_16x16x32_bf16 v[126:129], v[156:159], v[188:191], v[126:129]
	v_mfma_f32_16x16x32_bf16 v[122:125], v[164:167], v[188:191], v[122:125]
	v_mfma_f32_16x16x32_bf16 v[110:113], v[156:159], v[204:207], v[110:113]
	v_mfma_f32_16x16x32_bf16 v[106:109], v[164:167], v[204:207], v[106:109]
	v_mfma_f32_16x16x32_bf16 v[94:97], v[156:159], v[212:215], v[94:97]
	v_mfma_f32_16x16x32_bf16 v[90:93], v[164:167], v[212:215], v[90:93]
	v_mfma_f32_16x16x32_bf16 v[78:81], v[156:159], v[220:223], v[78:81]
	v_mfma_f32_16x16x32_bf16 v[74:77], v[164:167], v[220:223], v[74:77]
	v_mfma_f32_16x16x32_bf16 v[126:129], v[160:163], v[198:201], v[126:129]
	v_mfma_f32_16x16x32_bf16 v[122:125], v[168:171], v[198:201], v[122:125]
	v_mfma_f32_16x16x32_bf16 v[110:113], v[160:163], v[208:211], v[110:113]
	v_mfma_f32_16x16x32_bf16 v[106:109], v[168:171], v[208:211], v[106:109]
	v_mfma_f32_16x16x32_bf16 v[94:97], v[160:163], v[216:219], v[94:97]
	v_mfma_f32_16x16x32_bf16 v[90:93], v[168:171], v[216:219], v[90:93]
	v_mfma_f32_16x16x32_bf16 v[78:81], v[160:163], v[228:231], v[78:81]
	v_mfma_f32_16x16x32_bf16 v[74:77], v[168:171], v[228:231], v[74:77]
	s_setprio 0
	s_setprio 1
	v_mfma_f32_16x16x32_bf16 v[118:121], v[172:175], v[188:191], v[118:121]
	v_mfma_f32_16x16x32_bf16 v[114:117], v[180:183], v[188:191], v[114:117]
	v_mfma_f32_16x16x32_bf16 v[102:105], v[172:175], v[204:207], v[102:105]
	v_mfma_f32_16x16x32_bf16 v[98:101], v[180:183], v[204:207], v[98:101]
	v_mfma_f32_16x16x32_bf16 v[86:89], v[172:175], v[212:215], v[86:89]
	v_mfma_f32_16x16x32_bf16 v[82:85], v[180:183], v[212:215], v[82:85]
	v_mfma_f32_16x16x32_bf16 v[70:73], v[172:175], v[220:223], v[70:73]
	v_mfma_f32_16x16x32_bf16 v[66:69], v[180:183], v[220:223], v[66:69]
	v_mfma_f32_16x16x32_bf16 v[118:121], v[176:179], v[198:201], v[118:121]
	v_mfma_f32_16x16x32_bf16 v[114:117], v[184:187], v[198:201], v[114:117]
	v_mfma_f32_16x16x32_bf16 v[102:105], v[176:179], v[208:211], v[102:105]
	v_mfma_f32_16x16x32_bf16 v[98:101], v[184:187], v[208:211], v[98:101]
	v_mfma_f32_16x16x32_bf16 v[86:89], v[176:179], v[216:219], v[86:89]
	v_mfma_f32_16x16x32_bf16 v[82:85], v[184:187], v[216:219], v[82:85]
	v_mfma_f32_16x16x32_bf16 v[70:73], v[176:179], v[228:231], v[70:73]
	v_mfma_f32_16x16x32_bf16 v[66:69], v[184:187], v[228:231], v[66:69]
	s_setprio 0
	s_barrier
; #define PG8_STAGE_B(bufoff, gbase) do { _Pragma("unroll") for (int _i = 0; _i < 2; ++_i) \
;         __builtin_amdgcn_global_load_lds((const unsigned*)((const char*)(gbase) + voffB[_i]), (LAS unsigned*)(lds + (bufoff) + ldsw + _i * 8192), 16, 0, 0); } while (0)
; #define PG8_LDA(dst, b, h) do { _Pragma("unroll") for (int m = 0; m < 4; ++m) _Pragma("unroll") for (int k = 0; k < 2; ++k) dst[m][k] = *(const LAS bf16x8*)(lds + PG8_SA(b, h) + aoff + m * 2048 + k * 1024); } while (0)
; #define PG8_MMA(ai, bj, At, Bt) do { __builtin_amdgcn_s_setprio(1); _Pragma("unroll") for (int m = 0; m < 4; ++m) _Pragma("unroll") for (int n = 0; n < 2; ++n) _Pragma("unroll") for (int k = 0; k < 2; ++k) \
;         acc[ai][bj][m][n] = __builtin_amdgcn_mfma_f32_16x16x32_bf16(Bt[n][k], At[m][k], acc[ai][bj][m][n], 0, 0, 0); __builtin_amdgcn_s_setprio(0); } while (0)
; #define PG8_WAIT_V(n) asm volatile("s_waitcnt vmcnt(" #n ")" ::: "memory")
; #define PG8_WAIT_L(n) asm volatile("s_waitcnt lgkmcnt(" #n ")" ::: "memory")
; #define PG8_BAR __builtin_amdgcn_s_barrier()
; #define PG8_SCHED __builtin_amdgcn_sched_barrier(0)
; template <class Epi, class Sched, bool GATHER = false>
; __device__ __forceinline__ void gemm_phase(LAS unsigned char* lds, const Gemm g, const Sched& S, const Epi& E) {
;     ...
;             PG8_LDA(At, 1, 1); PG8_STAGE_B(PG8_SB(1, 0), b3); PG8_STAGE_B(PG8_SB(1, 1), b3 + hstepB); PG8_STAGE_A(PG8_SA(1, 0), a3, vo2, 0);
;             PG8_WAIT_V(8); PG8_WAIT_L(0); PG8_BAR; PG8_MMA(1, 0, At, B0); PG8_MMA(1, 1, At, B1); PG8_BAR; PG8_SCHED;
;         }
	s_add_i32 s30, s53, s40
	v_lshl_add_u64 v[236:237], v[236:237], 0, s[66:67]
	s_mov_b32 m0, s30
	ds_read_b128 v[188:191], v151 offset:49152
	ds_read_b128 v[198:201], v151 offset:50176
	ds_read_b128 v[204:207], v151 offset:51200
	ds_read_b128 v[208:211], v151 offset:52224
	ds_read_b128 v[212:215], v151 offset:53248
	ds_read_b128 v[216:219], v151 offset:54272
	ds_read_b128 v[220:223], v151 offset:55296
	ds_read_b128 v[228:231], v151 offset:56320
	global_load_lds_dwordx4 v[236:237], off
	s_add_i32 m0, s30, 0x2000
	s_add_u32 s28, s28, 0x40080
	v_lshl_add_u64 v[236:237], v[238:239], 0, s[66:67]
	s_addc_u32 s29, s29, 0
	s_add_i32 s30, s54, s40
	global_load_lds_dwordx4 v[236:237], off
	v_lshl_add_u64 v[236:237], s[28:29], 0, v[130:131]
	s_mov_b32 m0, s30
	v_lshl_add_u64 v[192:193], v[192:193], 0, s[66:67]
	global_load_lds_dwordx4 v[236:237], off
	v_lshl_add_u64 v[236:237], s[28:29], 0, v[132:133]
	s_add_i32 m0, s30, 0x2000
	s_nop 0
	global_load_lds_dwordx4 v[236:237], off
	v_lshl_add_u64 v[236:237], v[240:241], 0, s[66:67]
	s_mov_b32 m0, s44
	s_nop 0
	global_load_lds_dwordx4 v[236:237], off
	s_mov_b32 m0, s45
	s_nop 0
	global_load_lds_dwordx4 v[192:193], off
	s_waitcnt vmcnt(8)
	s_waitcnt lgkmcnt(0)
	s_barrier
	s_setprio 1
	s_waitcnt lgkmcnt(0)
	v_mfma_f32_16x16x32_bf16 v[62:65], v[156:159], v[188:191], v[62:65]
	v_mfma_f32_16x16x32_bf16 v[58:61], v[164:167], v[188:191], v[58:61]
	v_mfma_f32_16x16x32_bf16 v[46:49], v[156:159], v[204:207], v[46:49]
	v_mfma_f32_16x16x32_bf16 v[42:45], v[164:167], v[204:207], v[42:45]
	v_mfma_f32_16x16x32_bf16 v[30:33], v[156:159], v[212:215], v[30:33]
	v_mfma_f32_16x16x32_bf16 v[26:29], v[164:167], v[212:215], v[26:29]
	v_mfma_f32_16x16x32_bf16 v[14:17], v[156:159], v[220:223], v[14:17]
	v_mfma_f32_16x16x32_bf16 v[10:13], v[164:167], v[220:223], v[10:13]
	v_mfma_f32_16x16x32_bf16 v[62:65], v[160:163], v[198:201], v[62:65]
	v_mfma_f32_16x16x32_bf16 v[58:61], v[168:171], v[198:201], v[58:61]
	v_mfma_f32_16x16x32_bf16 v[46:49], v[160:163], v[208:211], v[46:49]
	v_mfma_f32_16x16x32_bf16 v[42:45], v[168:171], v[208:211], v[42:45]
	v_mfma_f32_16x16x32_bf16 v[30:33], v[160:163], v[216:219], v[30:33]
	v_mfma_f32_16x16x32_bf16 v[26:29], v[168:171], v[216:219], v[26:29]
	v_mfma_f32_16x16x32_bf16 v[14:17], v[160:163], v[228:231], v[14:17]
	v_mfma_f32_16x16x32_bf16 v[10:13], v[168:171], v[228:231], v[10:13]
	s_setprio 0
	s_setprio 1
	v_mfma_f32_16x16x32_bf16 v[54:57], v[172:175], v[188:191], v[54:57]
	v_mfma_f32_16x16x32_bf16 v[50:53], v[180:183], v[188:191], v[50:53]
	v_mfma_f32_16x16x32_bf16 v[38:41], v[172:175], v[204:207], v[38:41]
	v_mfma_f32_16x16x32_bf16 v[34:37], v[180:183], v[204:207], v[34:37]
	v_mfma_f32_16x16x32_bf16 v[22:25], v[172:175], v[212:215], v[22:25]
	v_mfma_f32_16x16x32_bf16 v[18:21], v[180:183], v[212:215], v[18:21]
	v_mfma_f32_16x16x32_bf16 v[6:9], v[172:175], v[220:223], v[6:9]
	v_mfma_f32_16x16x32_bf16 v[2:5], v[180:183], v[220:223], v[2:5]
	v_mfma_f32_16x16x32_bf16 v[54:57], v[176:179], v[198:201], v[54:57]
	v_mfma_f32_16x16x32_bf16 v[50:53], v[184:187], v[198:201], v[50:53]
	v_mfma_f32_16x16x32_bf16 v[38:41], v[176:179], v[208:211], v[38:41]
	v_mfma_f32_16x16x32_bf16 v[34:37], v[184:187], v[208:211], v[34:37]
	v_mfma_f32_16x16x32_bf16 v[22:25], v[176:179], v[216:219], v[22:25]
	v_mfma_f32_16x16x32_bf16 v[18:21], v[184:187], v[216:219], v[18:21]
	v_mfma_f32_16x16x32_bf16 v[6:9], v[176:179], v[228:231], v[6:9]
	v_mfma_f32_16x16x32_bf16 v[2:5], v[184:187], v[228:231], v[2:5]
	s_setprio 0
	s_barrier
	s_add_i32 s52, s52, 2
	s_add_u32 s26, s26, 0x100
	s_addc_u32 s27, s27, 0
	s_cmp_gt_u32 s52, 13
	s_cbranch_scc0 .LBB0_1402
	s_and_b64 vcc, exec, s[16:17]
	s_cbranch_vccz .LBB0_1405
	s_barrier
